# p0 prologue: the 32 per-row norm-gain loads of each fp8 weight item (gate/up 2 and wq) are issued together before the weight loads instead of one at a time behind vmcnt(0); on top of the memKV epilogu
# speedup vs baseline: 1.0077x; 1.0013x over previous
; #define LAS __attribute__((address_space(3)))
; #define LDS_WAIT() asm volatile("s_waitcnt lgkmcnt(0)" ::: "memory")
; __device__ __forceinline__ void tr_item8(const float* W, int Ns, unsigned char* WTrow, int K, int sc0, int k0, LAS float* scr, int lane, const float* gain = nullptr) {
;     const int col = lane & 31;
;     float wv_[32];
; #pragma unroll
;     for (int i = 0; i < 32; ++i) { const int kk = 2 * i + (lane >> 5); wv_[i] = W[(size_t)(k0 + kk) * Ns + sc0 + col]; }
; #pragma unroll
;     for (int i = 0; i < 32; ++i) { const int kk = 2 * i + (lane >> 5); float v = wv_[i] * 64.f; if (gain) v *= gain[k0 + kk]; scr[kk * 33 + col] = v; }
;     LDS_WAIT(); asm volatile("" ::: "memory");
; __device__ __forceinline__ void gu_item8(const float* wg, const float* wu, const float* gain, unsigned char* WT, int r, LAS float* scr, int lane) {
;     const int group = r >> 4, kb = r & 15, tile = group >> 3, g8 = group & 7;
;     tr_item8(g8 < 4 ? wg : wu, FF, WT + (size_t)(group * 32) * D + kb * 64, D, 128 * tile + 32 * (g8 & 3), kb * 64, scr, lane, gain);
.LBB0_53:
	s_and_b64 vcc, exec, s[4:5]
	s_cbranch_vccz .LBB0_122
	s_load_dwordx2 vcc, s[14:15], 0xb0
	s_and_b32 s4, s28, 0xf80
	s_bitcmp0_b32 s23, 6
	s_mul_i32 s16, s18, 0xb00000
	v_mov_b32_e32 v29, v5
	s_waitcnt lgkmcnt(0)
	s_cselect_b32 s10, s10, vcc_lo
	s_cselect_b32 s5, s11, vcc_hi
	s_mul_hi_i32 s11, s18, 0xb00000
	s_add_u32 s10, s10, s16
	s_addc_u32 s5, s5, s11
	s_add_i32 s11, s40, 0xfff7c000
	s_and_b32 s16, s11, 0x3c0
	s_lshl_b32 s11, s28, 1
	s_and_b32 s11, s11, 0x60
	s_or_b32 s4, s11, s4
	s_lshl_b32 s4, s4, 2
	s_add_u32 s4, s10, s4
	v_or_b32_e32 v24, s16, v11
	s_addc_u32 s5, s5, 0
	v_lshl_add_u64 v[22:23], s[4:5], 0, v[4:5]
	v_mul_u32_u24_e32 v28, 0x2c00, v24
	v_mad_u64_u32 v[26:27], s[4:5], v24, s73, v[22:23]
	v_lshl_add_u64 v[22:23], v[22:23], 0, v[28:29]
	v_add_co_u32_e32 v28, vcc, s74, v22
	s_cmp_lg_u64 s[8:9], 0
	s_nop 0
	v_addc_co_u32_e32 v29, vcc, 0, v23, vcc
	v_add_co_u32_e32 v30, vcc, s75, v22
	s_cselect_b64 s[10:11], -1, 0
	s_nop 0
	v_addc_co_u32_e32 v31, vcc, 0, v23, vcc
	v_add_co_u32_e32 v32, vcc, s48, v22
	s_cmp_eq_u64 s[8:9], 0
	s_nop 0
	v_addc_co_u32_e32 v33, vcc, 0, v23, vcc
	s_cbranch_scc1 .Lgha_skip
	v_add_lshl_u32 v160, s16, v11, 2
	global_load_dword v128, v160, s[20:21]
	global_load_dword v129, v160, s[20:21] offset:8
	global_load_dword v130, v160, s[20:21] offset:16
	global_load_dword v131, v160, s[20:21] offset:24
	global_load_dword v132, v160, s[20:21] offset:32
	global_load_dword v133, v160, s[20:21] offset:40
	global_load_dword v134, v160, s[20:21] offset:48
	global_load_dword v135, v160, s[20:21] offset:56
	global_load_dword v136, v160, s[20:21] offset:64
	global_load_dword v137, v160, s[20:21] offset:72
	global_load_dword v138, v160, s[20:21] offset:80
	global_load_dword v139, v160, s[20:21] offset:88
	global_load_dword v140, v160, s[20:21] offset:96
	global_load_dword v141, v160, s[20:21] offset:104
	global_load_dword v142, v160, s[20:21] offset:112
	global_load_dword v143, v160, s[20:21] offset:120
	global_load_dword v144, v160, s[20:21] offset:128
	global_load_dword v145, v160, s[20:21] offset:136
	global_load_dword v146, v160, s[20:21] offset:144
	global_load_dword v147, v160, s[20:21] offset:152
	global_load_dword v148, v160, s[20:21] offset:160
	global_load_dword v149, v160, s[20:21] offset:168
	global_load_dword v150, v160, s[20:21] offset:176
	global_load_dword v151, v160, s[20:21] offset:184
	global_load_dword v152, v160, s[20:21] offset:192
	global_load_dword v153, v160, s[20:21] offset:200
	global_load_dword v154, v160, s[20:21] offset:208
	global_load_dword v155, v160, s[20:21] offset:216
	global_load_dword v156, v160, s[20:21] offset:224
	global_load_dword v157, v160, s[20:21] offset:232
	global_load_dword v158, v160, s[20:21] offset:240
	global_load_dword v159, v160, s[20:21] offset:248
.Lgha_skip:
	v_add_co_u32_e32 v34, vcc, s51, v22
	s_nop 1
	v_addc_co_u32_e32 v35, vcc, 0, v23, vcc
	v_add_co_u32_e32 v36, vcc, s76, v22
	s_nop 1
	v_addc_co_u32_e32 v37, vcc, 0, v23, vcc
	v_add_co_u32_e32 v38, vcc, s77, v22
	s_nop 1
	v_addc_co_u32_e32 v39, vcc, 0, v23, vcc
	v_add_co_u32_e32 v40, vcc, s60, v22
	s_nop 1
	v_addc_co_u32_e32 v41, vcc, 0, v23, vcc
	global_load_dword v100, v[26:27], off
	global_load_dword v85, v[28:29], off offset:2048
	global_load_dword v84, v[30:31], off
	global_load_dword v83, v[32:33], off offset:2048
	global_load_dword v82, v[34:35], off
	global_load_dword v81, v[36:37], off offset:2048
	global_load_dword v79, v[38:39], off
	global_load_dword v77, v[40:41], off offset:2048
	v_add_co_u32_e32 v26, vcc, s63, v22
	s_nop 1
	v_addc_co_u32_e32 v27, vcc, 0, v23, vcc
	v_add_co_u32_e32 v28, vcc, s78, v22
	s_nop 1
	v_addc_co_u32_e32 v29, vcc, 0, v23, vcc
	v_add_co_u32_e32 v30, vcc, s79, v22
	s_nop 1
	v_addc_co_u32_e32 v31, vcc, 0, v23, vcc
	v_add_co_u32_e32 v32, vcc, s71, v22
	s_nop 1
	v_addc_co_u32_e32 v33, vcc, 0, v23, vcc
	v_add_co_u32_e32 v34, vcc, s80, v22
	s_nop 1
	v_addc_co_u32_e32 v35, vcc, 0, v23, vcc
	v_add_co_u32_e32 v36, vcc, s81, v22
	s_nop 1
	v_addc_co_u32_e32 v37, vcc, 0, v23, vcc
	v_add_co_u32_e32 v38, vcc, s82, v22
	s_nop 1
	v_addc_co_u32_e32 v39, vcc, 0, v23, vcc
	v_add_co_u32_e32 v86, vcc, s83, v22
	s_nop 1
	v_addc_co_u32_e32 v87, vcc, 0, v23, vcc
	global_load_dword v80, v[26:27], off
	global_load_dword v78, v[28:29], off offset:2048
	global_load_dword v76, v[30:31], off
	global_load_dword v75, v[32:33], off offset:2048
	global_load_dword v74, v[34:35], off
	global_load_dword v41, v[36:37], off offset:2048
	s_nop 0
	global_load_dword v39, v[38:39], off
	s_nop 0
	global_load_dword v37, v[86:87], off offset:2048
	v_add_co_u32_e32 v26, vcc, s84, v22
	s_nop 1
	v_addc_co_u32_e32 v27, vcc, 0, v23, vcc
	v_add_co_u32_e32 v28, vcc, s85, v22
	s_nop 1
	v_addc_co_u32_e32 v29, vcc, 0, v23, vcc
	v_add_co_u32_e32 v30, vcc, s86, v22
	s_nop 1
	v_addc_co_u32_e32 v31, vcc, 0, v23, vcc
	v_add_co_u32_e32 v32, vcc, s87, v22
	s_nop 1
	v_addc_co_u32_e32 v33, vcc, 0, v23, vcc
	v_add_co_u32_e32 v86, vcc, s88, v22
	s_nop 1
	v_addc_co_u32_e32 v87, vcc, 0, v23, vcc
	v_add_co_u32_e32 v88, vcc, s89, v22
	s_nop 1
	v_addc_co_u32_e32 v89, vcc, 0, v23, vcc
	v_add_co_u32_e32 v90, vcc, s90, v22
	s_nop 1
	v_addc_co_u32_e32 v91, vcc, 0, v23, vcc
	v_add_co_u32_e32 v92, vcc, s91, v22
	s_nop 1
	v_addc_co_u32_e32 v93, vcc, 0, v23, vcc
	global_load_dword v40, v[26:27], off
	global_load_dword v38, v[28:29], off offset:2048
	global_load_dword v36, v[30:31], off
	global_load_dword v35, v[32:33], off offset:2048
	global_load_dword v34, v[86:87], off
	s_nop 0
	global_load_dword v32, v[88:89], off offset:2048
	global_load_dword v30, v[90:91], off
	global_load_dword v28, v[92:93], off offset:2048
	v_add_co_u32_e32 v26, vcc, s92, v22
	s_nop 1
	v_addc_co_u32_e32 v27, vcc, 0, v23, vcc
	v_add_co_u32_e32 v86, vcc, s93, v22
	s_nop 1
	v_addc_co_u32_e32 v87, vcc, 0, v23, vcc
	v_add_co_u32_e32 v88, vcc, s94, v22
	s_nop 1
	v_addc_co_u32_e32 v89, vcc, 0, v23, vcc
	v_add_co_u32_e32 v90, vcc, s95, v22
	s_nop 1
	v_addc_co_u32_e32 v91, vcc, 0, v23, vcc
	v_add_co_u32_e32 v92, vcc, s96, v22
	s_nop 1
	v_addc_co_u32_e32 v93, vcc, 0, v23, vcc
	v_add_co_u32_e32 v94, vcc, s97, v22
	s_nop 1
	v_addc_co_u32_e32 v95, vcc, 0, v23, vcc
	v_add_co_u32_e32 v96, vcc, 0xa5000, v22
	s_nop 1
	v_addc_co_u32_e32 v97, vcc, 0, v23, vcc
	v_add_co_u32_e32 v98, vcc, 0xaa000, v22
	s_nop 1
	v_addc_co_u32_e32 v99, vcc, 0, v23, vcc
	global_load_dword v33, v[26:27], off
	global_load_dword v31, v[86:87], off offset:2048
	global_load_dword v29, v[88:89], off
	s_nop 0
	global_load_dword v27, v[90:91], off offset:2048
	global_load_dword v26, v[92:93], off
	global_load_dword v25, v[94:95], off offset:2048
	global_load_dword v23, v[96:97], off
	global_load_dword v22, v[98:99], off offset:2048
	s_waitcnt vmcnt(31)
	v_mul_f32_e32 v86, 0x42800000, v100
	s_cbranch_scc1 .LBB0_56
	v_lshlrev_b32_e32 v24, 2, v24
	v_mul_f32_e32 v86, v86, v128
; #define LDS_WAIT() asm volatile("s_waitcnt lgkmcnt(0)" ::: "memory")
; __device__ __forceinline__ void tr_item8(const float* W, int Ns, unsigned char* WTrow, int K, int sc0, int k0, LAS float* scr, int lane, const float* gain = nullptr) {
;     ...
;     for (int i = 0; i < 32; ++i) { const int kk = 2 * i + (lane >> 5); wv_[i] = W[(size_t)(k0 + kk) * Ns + sc0 + col]; }
; #pragma unroll
;     for (int i = 0; i < 32; ++i) { const int kk = 2 * i + (lane >> 5); float v = wv_[i] * 64.f; if (gain) v *= gain[k0 + kk]; scr[kk * 33 + col] = v; }
;     LDS_WAIT(); asm volatile("" ::: "memory");
.LBB0_56:
	v_cndmask_b32_e64 v24, 0, 1, s[10:11]
	s_waitcnt vmcnt(30)
	v_mul_f32_e32 v85, 0x42800000, v85
	v_cmp_ne_u32_e64 s[4:5], 1, v24
	s_andn2_b64 vcc, exec, s[10:11]
	v_add_lshl_u32 v24, s16, v11, 2
	ds_write_b32 v43, v86
	s_cbranch_vccnz .LBB0_58
	v_mul_f32_e32 v85, v85, v129
.LBB0_58:
	v_add_u32_e32 v86, v42, v45
	s_and_b64 vcc, exec, s[4:5]
	s_waitcnt vmcnt(29)
	v_mul_f32_e32 v84, 0x42800000, v84
	ds_write_b32 v86, v85
	s_cbranch_vccnz .LBB0_60
	v_mul_f32_e32 v84, v84, v130
.LBB0_60:
	v_add_u32_e32 v85, v42, v46
	s_and_b64 vcc, exec, s[4:5]
	s_waitcnt vmcnt(28)
	v_mul_f32_e32 v83, 0x42800000, v83
	ds_write_b32 v85, v84
	s_cbranch_vccnz .LBB0_62
	v_mul_f32_e32 v83, v83, v131
.LBB0_62:
	v_add_u32_e32 v84, v42, v47
	s_and_b64 vcc, exec, s[4:5]
	s_waitcnt vmcnt(27)
	v_mul_f32_e32 v82, 0x42800000, v82
	ds_write_b32 v84, v83
	s_cbranch_vccnz .LBB0_64
	v_mul_f32_e32 v82, v82, v132
.LBB0_64:
	v_add_u32_e32 v83, v42, v48
	s_and_b64 vcc, exec, s[4:5]
	s_waitcnt vmcnt(26)
	v_mul_f32_e32 v81, 0x42800000, v81
	ds_write_b32 v83, v82
	s_cbranch_vccnz .LBB0_66
	v_mul_f32_e32 v81, v81, v133
.LBB0_66:
	v_add_u32_e32 v82, v42, v49
	s_and_b64 vcc, exec, s[4:5]
	s_waitcnt vmcnt(25)
	v_mul_f32_e32 v79, 0x42800000, v79
	ds_write_b32 v82, v81
	s_cbranch_vccnz .LBB0_68
	v_mul_f32_e32 v79, v79, v134
.LBB0_68:
	v_add_u32_e32 v81, v42, v50
	s_and_b64 vcc, exec, s[4:5]
	s_waitcnt vmcnt(24)
	v_mul_f32_e32 v77, 0x42800000, v77
	ds_write_b32 v81, v79
	s_cbranch_vccnz .LBB0_70
	v_mul_f32_e32 v77, v77, v135
.LBB0_70:
	v_add_u32_e32 v79, v42, v51
	ds_write_b32 v79, v77
	s_and_b64 vcc, exec, s[4:5]
	s_waitcnt vmcnt(23)
	v_mul_f32_e32 v77, 0x42800000, v80
	s_cbranch_vccnz .LBB0_72
	v_mul_f32_e32 v77, v77, v136
.LBB0_72:
	v_add_u32_e32 v79, v42, v52
	ds_write_b32 v79, v77
	s_and_b64 vcc, exec, s[4:5]
	s_waitcnt vmcnt(22)
	v_mul_f32_e32 v77, 0x42800000, v78
	s_cbranch_vccnz .LBB0_74
	v_mul_f32_e32 v77, v77, v137
.LBB0_74:
	v_add_u32_e32 v78, v42, v53
	s_and_b64 vcc, exec, s[4:5]
	s_waitcnt vmcnt(21)
	v_mul_f32_e32 v76, 0x42800000, v76
	ds_write_b32 v78, v77
	s_cbranch_vccnz .LBB0_76
	v_mul_f32_e32 v76, v76, v138
.LBB0_76:
	v_add_u32_e32 v77, v42, v54
	s_and_b64 vcc, exec, s[4:5]
	s_waitcnt vmcnt(20)
	v_mul_f32_e32 v75, 0x42800000, v75
	ds_write_b32 v77, v76
	s_cbranch_vccnz .LBB0_78
	v_mul_f32_e32 v75, v75, v139
.LBB0_78:
	v_add_u32_e32 v76, v42, v55
	s_and_b64 vcc, exec, s[4:5]
	s_waitcnt vmcnt(19)
	v_mul_f32_e32 v74, 0x42800000, v74
	ds_write_b32 v76, v75
	s_cbranch_vccnz .LBB0_80
	v_mul_f32_e32 v74, v74, v140
.LBB0_80:
	v_add_u32_e32 v75, v42, v56
	s_and_b64 vcc, exec, s[4:5]
	s_waitcnt vmcnt(18)
	v_mul_f32_e32 v41, 0x42800000, v41
	ds_write_b32 v75, v74
	s_cbranch_vccnz .LBB0_82
	v_mul_f32_e32 v41, v41, v141
.LBB0_82:
	v_add_u32_e32 v74, v42, v57
	s_and_b64 vcc, exec, s[4:5]
	s_waitcnt vmcnt(17)
	v_mul_f32_e32 v39, 0x42800000, v39
	ds_write_b32 v74, v41
	s_cbranch_vccnz .LBB0_84
	v_mul_f32_e32 v39, v39, v142
.LBB0_84:
	v_add_u32_e32 v41, v42, v58
	s_and_b64 vcc, exec, s[4:5]
	s_waitcnt vmcnt(16)
	v_mul_f32_e32 v37, 0x42800000, v37
	ds_write_b32 v41, v39
	s_cbranch_vccnz .LBB0_86
	v_mul_f32_e32 v37, v37, v143
.LBB0_86:
	v_add_u32_e32 v39, v42, v59
	ds_write_b32 v39, v37
	s_and_b64 vcc, exec, s[4:5]
	s_waitcnt vmcnt(15)
	v_mul_f32_e32 v37, 0x42800000, v40
	s_cbranch_vccnz .LBB0_88
	v_mul_f32_e32 v37, v37, v144
.LBB0_88:
	v_add_u32_e32 v39, v42, v60
	ds_write_b32 v39, v37
	s_and_b64 vcc, exec, s[4:5]
	s_waitcnt vmcnt(14)
	v_mul_f32_e32 v37, 0x42800000, v38
	s_cbranch_vccnz .LBB0_90
	v_mul_f32_e32 v37, v37, v145
.LBB0_90:
	v_add_u32_e32 v38, v42, v61
	s_and_b64 vcc, exec, s[4:5]
	s_waitcnt vmcnt(13)
	v_mul_f32_e32 v36, 0x42800000, v36
	ds_write_b32 v38, v37
	s_cbranch_vccnz .LBB0_92
	v_mul_f32_e32 v36, v36, v146
.LBB0_92:
	v_add_u32_e32 v37, v42, v62
	s_and_b64 vcc, exec, s[4:5]
	s_waitcnt vmcnt(12)
	v_mul_f32_e32 v35, 0x42800000, v35
	ds_write_b32 v37, v36
	s_cbranch_vccnz .LBB0_94
	v_mul_f32_e32 v35, v35, v147
.LBB0_94:
	v_add_u32_e32 v36, v42, v63
	s_and_b64 vcc, exec, s[4:5]
	s_waitcnt vmcnt(11)
	v_mul_f32_e32 v34, 0x42800000, v34
	ds_write_b32 v36, v35
	s_cbranch_vccnz .LBB0_96
	v_mul_f32_e32 v34, v34, v148
.LBB0_96:
	v_add_u32_e32 v35, v42, v64
	s_and_b64 vcc, exec, s[4:5]
	s_waitcnt vmcnt(10)
	v_mul_f32_e32 v32, 0x42800000, v32
	ds_write_b32 v35, v34
	s_cbranch_vccnz .LBB0_98
	v_mul_f32_e32 v32, v32, v149
.LBB0_98:
	v_add_u32_e32 v34, v42, v65
	s_and_b64 vcc, exec, s[4:5]
	s_waitcnt vmcnt(9)
	v_mul_f32_e32 v30, 0x42800000, v30
	ds_write_b32 v34, v32
	s_cbranch_vccnz .LBB0_100
	v_mul_f32_e32 v30, v30, v150
.LBB0_100:
	v_add_u32_e32 v32, v42, v66
	s_and_b64 vcc, exec, s[4:5]
	s_waitcnt vmcnt(8)
	v_mul_f32_e32 v28, 0x42800000, v28
	ds_write_b32 v32, v30
	s_cbranch_vccnz .LBB0_102
	v_mul_f32_e32 v28, v28, v151
.LBB0_102:
	v_add_u32_e32 v30, v42, v67
	ds_write_b32 v30, v28
	s_and_b64 vcc, exec, s[4:5]
	s_waitcnt vmcnt(7)
	v_mul_f32_e32 v30, 0x42800000, v33
	s_cbranch_vccnz .LBB0_104
	v_mul_f32_e32 v30, v30, v152
.LBB0_104:
	v_add_u32_e32 v28, v42, v68
	ds_write_b32 v28, v30
	s_and_b64 vcc, exec, s[4:5]
	s_waitcnt vmcnt(6)
	v_mul_f32_e32 v30, 0x42800000, v31
	s_cbranch_vccnz .LBB0_106
	v_mul_f32_e32 v30, v30, v153
.LBB0_106:
	s_and_b64 vcc, exec, s[4:5]
	s_waitcnt vmcnt(5)
	v_mul_f32_e32 v29, 0x42800000, v29
	ds_write_b32 v28, v30 offset:264
	s_cbranch_vccnz .LBB0_108
	v_mul_f32_e32 v29, v29, v154
.LBB0_108:
	s_and_b64 vcc, exec, s[4:5]
	s_waitcnt vmcnt(4)
	v_mul_f32_e32 v27, 0x42800000, v27
	ds_write_b32 v28, v29 offset:528
	s_cbranch_vccnz .LBB0_110
	v_mul_f32_e32 v27, v27, v155
.LBB0_110:
	s_and_b64 vcc, exec, s[4:5]
	s_waitcnt vmcnt(3)
	v_mul_f32_e32 v26, 0x42800000, v26
	ds_write_b32 v28, v27 offset:792
	s_cbranch_vccnz .LBB0_112
	v_mul_f32_e32 v26, v26, v156
.LBB0_112:
	s_and_b64 vcc, exec, s[4:5]
	s_waitcnt vmcnt(2)
	v_mul_f32_e32 v25, 0x42800000, v25
	ds_write_b32 v28, v26 offset:1056
	s_cbranch_vccnz .LBB0_114
	v_mul_f32_e32 v25, v25, v157
.LBB0_114:
	s_and_b64 vcc, exec, s[4:5]
	s_waitcnt vmcnt(1)
	v_mul_f32_e32 v23, 0x42800000, v23
	ds_write_b32 v28, v25 offset:1320
	s_cbranch_vccnz .LBB0_116
	v_mul_f32_e32 v23, v23, v158
.LBB0_116:
	s_waitcnt vmcnt(0)
	v_mul_f32_e32 v22, 0x42800000, v22
	s_and_b64 vcc, exec, s[10:11]
	ds_write_b32 v28, v23 offset:1584
	s_cbranch_vccz .LBB0_118
	s_mov_b64 s[4:5], 0
	v_mul_f32_e32 v23, v22, v159
	s_branch .LBB0_119

; #define LAS __attribute__((address_space(3)))
; #define LDS_WAIT() asm volatile("s_waitcnt lgkmcnt(0)" ::: "memory")
; __device__ __forceinline__ void tr_item8(const float* W, int Ns, unsigned char* WTrow, int K, int sc0, int k0, LAS float* scr, int lane, const float* gain = nullptr) {
;     const int col = lane & 31;
;     float wv_[32];
; #pragma unroll
;     for (int i = 0; i < 32; ++i) { const int kk = 2 * i + (lane >> 5); wv_[i] = W[(size_t)(k0 + kk) * Ns + sc0 + col]; }
; #pragma unroll
;     for (int i = 0; i < 32; ++i) { const int kk = 2 * i + (lane >> 5); float v = wv_[i] * 64.f; if (gain) v *= gain[k0 + kk]; scr[kk * 33 + col] = v; }
;     LDS_WAIT(); asm volatile("" ::: "memory");
; __device__ __forceinline__ void plain_item8(const float* W, int Ns, int K, unsigned char* WT, int r, LAS float* scr, int lane, const float* gain = nullptr) {
;     const int nkb = K / 64, group = r / nkb, kb = r % nkb;
;     tr_item8(W, Ns, WT + (size_t)(group * 32) * K + kb * 64, K, group * 32, kb * 64, scr, lane, gain);
.LBB0_141:
	s_andn2_b64 vcc, exec, s[4:5]
	s_cbranch_vccnz .LBB0_207
	s_waitcnt lgkmcnt(0)
	s_load_dwordx2 s[8:9], s[14:15], 0x88
	s_load_dwordx2 s[4:5], s[14:15], 0x78
	s_lshl_b64 s[10:11], s[18:19], 22
	v_mov_b32_e32 v27, v5
	s_waitcnt lgkmcnt(0)
	s_add_u32 s10, s8, s10
	s_addc_u32 s11, s9, s11
	s_lshl_b32 s8, s18, 10
	s_ashr_i32 s9, s8, 31
	s_lshl_b64 s[8:9], s[8:9], 2
	s_add_u32 s8, s4, s8
	s_addc_u32 s9, s5, s9
	s_lshl_b32 s16, s23, 1
	s_and_b32 s16, s16, 0x3fe0
	s_add_i32 s20, s16, 0xce00
	s_lshl_b32 s16, s23, 6
	s_and_b32 s20, s20, 0xffe0
	s_and_b32 s16, s16, 0x3c0
	s_lshl_b32 s21, s20, 2
	s_add_u32 s10, s10, s21
	v_or_b32_e32 v24, s16, v11
	s_addc_u32 s11, s11, 0
	v_lshl_add_u64 v[22:23], s[10:11], 0, v[4:5]
	v_lshlrev_b32_e32 v26, 12, v24
	v_lshl_add_u64 v[22:23], v[22:23], 0, v[26:27]
	v_add_co_u32_e32 v26, vcc, s72, v22
	s_mov_b32 s10, 0xe000
	s_nop 0
	v_addc_co_u32_e32 v27, vcc, 0, v23, vcc
	v_add_co_u32_e32 v28, vcc, s35, v22
	s_cmp_lg_u64 s[4:5], 0
	s_nop 0
	v_addc_co_u32_e32 v29, vcc, 0, v23, vcc
	v_add_co_u32_e32 v30, vcc, s28, v22
	s_nop 1
	v_addc_co_u32_e32 v31, vcc, 0, v23, vcc
	v_add_co_u32_e32 v32, vcc, s36, v22
	s_nop 1
	v_addc_co_u32_e32 v33, vcc, 0, v23, vcc
	v_add_co_u32_e32 v34, vcc, s29, v22
	s_nop 1
	v_addc_co_u32_e32 v35, vcc, 0, v23, vcc
	v_add_co_u32_e32 v36, vcc, s37, v22
	s_nop 1
	v_addc_co_u32_e32 v37, vcc, 0, v23, vcc
	v_add_co_u32_e32 v38, vcc, s10, v22
	s_cselect_b64 s[10:11], -1, 0
	s_nop 0
	v_addc_co_u32_e32 v39, vcc, 0, v23, vcc
	global_load_dword v100, v[22:23], off
	global_load_dword v85, v[26:27], off
	global_load_dword v84, v[28:29], off
	global_load_dword v83, v[30:31], off
	global_load_dword v82, v[32:33], off
	global_load_dword v81, v[34:35], off
	global_load_dword v79, v[36:37], off
	global_load_dword v77, v[38:39], off
	v_add_co_u32_e32 v26, vcc, s48, v22
	s_cmp_eq_u64 s[4:5], 0
	s_nop 0
	v_addc_co_u32_e32 v27, vcc, 0, v23, vcc
	s_cbranch_scc1 .Lghb_skip
	v_add_lshl_u32 v160, s16, v11, 2
	global_load_dword v128, v160, s[8:9]
	global_load_dword v129, v160, s[8:9] offset:8
	global_load_dword v130, v160, s[8:9] offset:16
	global_load_dword v131, v160, s[8:9] offset:24
	global_load_dword v132, v160, s[8:9] offset:32
	global_load_dword v133, v160, s[8:9] offset:40
	global_load_dword v134, v160, s[8:9] offset:48
	global_load_dword v135, v160, s[8:9] offset:56
	global_load_dword v136, v160, s[8:9] offset:64
	global_load_dword v137, v160, s[8:9] offset:72
	global_load_dword v138, v160, s[8:9] offset:80
	global_load_dword v139, v160, s[8:9] offset:88
	global_load_dword v140, v160, s[8:9] offset:96
	global_load_dword v141, v160, s[8:9] offset:104
	global_load_dword v142, v160, s[8:9] offset:112
	global_load_dword v143, v160, s[8:9] offset:120
	global_load_dword v144, v160, s[8:9] offset:128
	global_load_dword v145, v160, s[8:9] offset:136
	global_load_dword v146, v160, s[8:9] offset:144
	global_load_dword v147, v160, s[8:9] offset:152
	global_load_dword v148, v160, s[8:9] offset:160
	global_load_dword v149, v160, s[8:9] offset:168
	global_load_dword v150, v160, s[8:9] offset:176
	global_load_dword v151, v160, s[8:9] offset:184
	global_load_dword v152, v160, s[8:9] offset:192
	global_load_dword v153, v160, s[8:9] offset:200
	global_load_dword v154, v160, s[8:9] offset:208
	global_load_dword v155, v160, s[8:9] offset:216
	global_load_dword v156, v160, s[8:9] offset:224
	global_load_dword v157, v160, s[8:9] offset:232
	global_load_dword v158, v160, s[8:9] offset:240
	global_load_dword v159, v160, s[8:9] offset:248
.Lghb_skip:
	v_add_co_u32_e32 v28, vcc, s49, v22
	s_nop 1
	v_addc_co_u32_e32 v29, vcc, 0, v23, vcc
	v_add_co_u32_e32 v30, vcc, s50, v22
	s_nop 1
	v_addc_co_u32_e32 v31, vcc, 0, v23, vcc
	v_add_co_u32_e32 v32, vcc, s51, v22
	s_nop 1
	v_addc_co_u32_e32 v33, vcc, 0, v23, vcc
	v_add_co_u32_e32 v34, vcc, s53, v22
	s_nop 1
	v_addc_co_u32_e32 v35, vcc, 0, v23, vcc
	v_add_co_u32_e32 v36, vcc, s54, v22
	s_nop 1
	v_addc_co_u32_e32 v37, vcc, 0, v23, vcc
	v_add_co_u32_e32 v38, vcc, s55, v22
	s_nop 1
	v_addc_co_u32_e32 v39, vcc, 0, v23, vcc
	v_add_co_u32_e32 v86, vcc, s56, v22
	s_nop 1
	v_addc_co_u32_e32 v87, vcc, 0, v23, vcc
	global_load_dword v80, v[26:27], off
	global_load_dword v78, v[28:29], off
	global_load_dword v76, v[30:31], off
	global_load_dword v75, v[32:33], off
	global_load_dword v74, v[34:35], off
	global_load_dword v41, v[36:37], off
	s_nop 0
	global_load_dword v39, v[38:39], off
	s_nop 0
	global_load_dword v37, v[86:87], off
	v_add_co_u32_e32 v26, vcc, s57, v22
	s_nop 1
	v_addc_co_u32_e32 v27, vcc, 0, v23, vcc
	v_add_co_u32_e32 v28, vcc, s58, v22
	s_nop 1
	v_addc_co_u32_e32 v29, vcc, 0, v23, vcc
	v_add_co_u32_e32 v30, vcc, s59, v22
	s_nop 1
	v_addc_co_u32_e32 v31, vcc, 0, v23, vcc
	v_add_co_u32_e32 v32, vcc, s60, v22
	s_nop 1
	v_addc_co_u32_e32 v33, vcc, 0, v23, vcc
	v_add_co_u32_e32 v86, vcc, s61, v22
	s_nop 1
	v_addc_co_u32_e32 v87, vcc, 0, v23, vcc
	v_add_co_u32_e32 v88, vcc, s62, v22
	s_nop 1
	v_addc_co_u32_e32 v89, vcc, 0, v23, vcc
	v_add_co_u32_e32 v90, vcc, s63, v22
	s_nop 1
	v_addc_co_u32_e32 v91, vcc, 0, v23, vcc
	v_add_co_u32_e32 v92, vcc, s64, v22
	s_nop 1
	v_addc_co_u32_e32 v93, vcc, 0, v23, vcc
	global_load_dword v40, v[26:27], off
	global_load_dword v38, v[28:29], off
	global_load_dword v36, v[30:31], off
	global_load_dword v35, v[32:33], off
	global_load_dword v34, v[86:87], off
	s_nop 0
	global_load_dword v32, v[88:89], off
	global_load_dword v30, v[90:91], off
	global_load_dword v28, v[92:93], off
	v_add_co_u32_e32 v26, vcc, s65, v22
	s_nop 1
	v_addc_co_u32_e32 v27, vcc, 0, v23, vcc
	v_add_co_u32_e32 v86, vcc, s66, v22
	s_nop 1
	v_addc_co_u32_e32 v87, vcc, 0, v23, vcc
	v_add_co_u32_e32 v88, vcc, s67, v22
	s_nop 1
	v_addc_co_u32_e32 v89, vcc, 0, v23, vcc
	v_add_co_u32_e32 v90, vcc, s68, v22
	s_nop 1
	v_addc_co_u32_e32 v91, vcc, 0, v23, vcc
	v_add_co_u32_e32 v92, vcc, s69, v22
	s_nop 1
	v_addc_co_u32_e32 v93, vcc, 0, v23, vcc
	v_add_co_u32_e32 v94, vcc, s70, v22
	s_nop 1
	v_addc_co_u32_e32 v95, vcc, 0, v23, vcc
	v_add_co_u32_e32 v96, vcc, 0x3c000, v22
	s_nop 1
	v_addc_co_u32_e32 v97, vcc, 0, v23, vcc
	v_add_co_u32_e32 v98, vcc, 0x3e000, v22
	s_nop 1
	v_addc_co_u32_e32 v99, vcc, 0, v23, vcc
	global_load_dword v33, v[26:27], off
	global_load_dword v31, v[86:87], off
	global_load_dword v29, v[88:89], off
	s_nop 0
	global_load_dword v27, v[90:91], off
	global_load_dword v26, v[92:93], off
	global_load_dword v25, v[94:95], off
	global_load_dword v23, v[96:97], off
	global_load_dword v22, v[98:99], off
	s_waitcnt vmcnt(31)
	v_mul_f32_e32 v86, 0x42800000, v100
	s_cbranch_scc1 .LBB0_144
	v_lshlrev_b32_e32 v24, 2, v24
	v_mul_f32_e32 v86, v86, v128
.LBB0_144:
	v_cndmask_b32_e64 v24, 0, 1, s[10:11]
	s_waitcnt vmcnt(30)
	v_mul_f32_e32 v85, 0x42800000, v85
	v_cmp_ne_u32_e64 s[4:5], 1, v24
	s_andn2_b64 vcc, exec, s[10:11]
	v_add_lshl_u32 v24, v11, s16, 2
	ds_write_b32 v43, v86
	s_cbranch_vccnz .LBB0_146
	v_mul_f32_e32 v85, v85, v129

; #define LDS_WAIT() asm volatile("s_waitcnt lgkmcnt(0)" ::: "memory")
; __device__ __forceinline__ void tr_item8(const float* W, int Ns, unsigned char* WTrow, int K, int sc0, int k0, LAS float* scr, int lane, const float* gain = nullptr) {
;     ...
;     for (int i = 0; i < 32; ++i) { const int kk = 2 * i + (lane >> 5); float v = wv_[i] * 64.f; if (gain) v *= gain[k0 + kk]; scr[kk * 33 + col] = v; }
;     LDS_WAIT(); asm volatile("" ::: "memory");
.LBB0_204:
	s_and_b64 vcc, exec, s[4:5]
	s_waitcnt vmcnt(0)
	v_mul_f32_e32 v22, 0x42800000, v22
	ds_write_b32 v28, v23 offset:1584
	s_cbranch_vccnz .LBB0_206
	v_mul_f32_e32 v22, v22, v159
